# baseline (speedup 1.0000x reference)
.LBB3_3:
	s_waitcnt vmcnt(0)
	v_mfma_f32_32x32x16_f16 v[18:33], v[78:81], v[66:69], 0
	v_add_u32_e32 v149, s3, v89
	v_lshl_add_u32 v4, v149, 2, v147
	ds_read2_b32 v[122:123], v4 offset1:16
	ds_read2_b32 v[98:99], v4 offset0:32 offset1:48
	ds_read2_b32 v[100:101], v4 offset0:64 offset1:80
	ds_read2_b32 v[102:103], v4 offset0:96 offset1:112
	ds_read2_b32 v[104:105], v4 offset0:128 offset1:144
	ds_read2_b32 v[106:107], v4 offset0:160 offset1:176
	ds_read2_b32 v[110:111], v4 offset0:224 offset1:240
	ds_read2_b32 v[108:109], v4 offset0:192 offset1:208
	s_nop 1
	v_exp_f32_e32 v2, v18
	v_exp_f32_e32 v3, v19
	v_mfma_f32_32x32x16_f16 v[34:49], v[78:81], v[54:57], 0
	v_exp_f32_e32 v120, v26
	v_exp_f32_e32 v121, v27
	v_pk_add_f32 v[2:3], v[2:3], 1.0 op_sel_hi:[1,0]
	v_exp_f32_e32 v126, v30
	v_log_f32_e32 v112, v2
	v_log_f32_e32 v113, v3
	v_exp_f32_e32 v127, v31
	s_waitcnt lgkmcnt(6)
	s_nop 3
	v_pk_mul_f32 v[36:37], v[98:99], v[36:37]
	s_waitcnt lgkmcnt(5)
	v_pk_mul_f32 v[38:39], v[100:101], v[38:39]
	v_pk_mul_f32 v[2:3], v[96:97], v[112:113]
	s_waitcnt lgkmcnt(4)
	v_pk_mul_f32 v[40:41], v[102:103], v[40:41]
	v_exp_f32_e32 v114, v2
	v_exp_f32_e32 v115, v3
	v_mfma_f32_32x32x16_f16 v[2:17], v[78:81], v[50:53], 0
	v_exp_f32_e32 v80, v20
	v_exp_f32_e32 v81, v21
	v_pk_mul_f32 v[78:79], v[122:123], v[34:35]
	s_waitcnt lgkmcnt(3)
	v_pk_mul_f32 v[42:43], v[104:105], v[42:43]
	v_pk_mul_f32 v[118:119], v[78:79], v[112:113]
	v_pk_add_f32 v[34:35], v[80:81], 1.0 op_sel_hi:[1,0]
	v_fma_mix_f32 v118, v114, v151, v118 op_sel_hi:[0,1,0]
	v_log_f32_e32 v34, v34
	v_log_f32_e32 v35, v35
	v_fmac_f32_e32 v119, v115, v118
	v_exp_f32_e32 v114, v22
	v_exp_f32_e32 v115, v23
	v_pk_mul_f32 v[80:81], v[96:97], v[34:35]
	v_pk_mul_f32 v[128:129], v[36:37], v[34:35]
	v_exp_f32_e32 v80, v80
	v_exp_f32_e32 v116, v81
	s_waitcnt lgkmcnt(2)
	v_pk_mul_f32 v[44:45], v[106:107], v[44:45]
	s_waitcnt lgkmcnt(0)
	v_pk_mul_f32 v[46:47], v[108:109], v[46:47]
	v_fma_f32 v128, v80, v119, v128
	v_pk_add_f32 v[80:81], v[114:115], 1.0 op_sel_hi:[1,0]
	v_exp_f32_e32 v114, v24
	v_log_f32_e32 v80, v80
	v_log_f32_e32 v81, v81
	v_exp_f32_e32 v115, v25
	v_fmac_f32_e32 v129, v116, v128
	v_pk_mul_f32 v[48:49], v[110:111], v[48:49]
	v_pk_mul_f32 v[116:117], v[96:97], v[80:81]
	v_pk_add_f32 v[114:115], v[114:115], 1.0 op_sel_hi:[1,0]
	v_exp_f32_e32 v116, v116
	v_exp_f32_e32 v117, v117
	v_log_f32_e32 v114, v114
	v_log_f32_e32 v115, v115
	v_pk_mul_f32 v[130:131], v[38:39], v[80:81]
	v_pk_mul_f32 v[132:133], v[40:41], v[114:115]
	v_fma_f32 v130, v116, v129, v130
	v_fmac_f32_e32 v131, v117, v130
	v_pk_mul_f32 v[116:117], v[96:97], v[114:115]
	s_nop 0
	v_exp_f32_e32 v116, v116
	v_exp_f32_e32 v124, v117
	v_fma_f32 v132, v116, v131, v132
	v_pk_add_f32 v[116:117], v[120:121], 1.0 op_sel_hi:[1,0]
	v_exp_f32_e32 v120, v28
	v_log_f32_e32 v116, v116
	v_log_f32_e32 v117, v117
	v_exp_f32_e32 v121, v29
	v_fmac_f32_e32 v133, v124, v132
	v_pk_mul_f32 v[124:125], v[96:97], v[116:117]
	s_nop 0
	v_exp_f32_e32 v124, v124
	v_pk_add_f32 v[120:121], v[120:121], 1.0 op_sel_hi:[1,0]
	v_exp_f32_e32 v125, v125
	v_log_f32_e32 v120, v120
	v_log_f32_e32 v121, v121
	v_pk_mul_f32 v[134:135], v[42:43], v[116:117]
	v_pk_mul_f32 v[136:137], v[44:45], v[120:121]
	v_fma_f32 v134, v124, v133, v134
	v_fmac_f32_e32 v135, v125, v134
	v_pk_mul_f32 v[124:125], v[96:97], v[120:121]
	s_nop 0
	v_exp_f32_e32 v124, v124
	v_exp_f32_e32 v138, v125
	v_fma_f32 v136, v124, v135, v136
	v_pk_add_f32 v[124:125], v[126:127], 1.0 op_sel_hi:[1,0]
	v_exp_f32_e32 v126, v32
	v_log_f32_e32 v124, v124
	v_log_f32_e32 v125, v125
	v_exp_f32_e32 v127, v33
	v_fmac_f32_e32 v137, v138, v136
	v_pk_mul_f32 v[138:139], v[96:97], v[124:125]
	v_pk_add_f32 v[126:127], v[126:127], 1.0 op_sel_hi:[1,0]
	v_exp_f32_e32 v140, v138
	v_log_f32_e32 v126, v126
	v_log_f32_e32 v127, v127
	v_exp_f32_e32 v152, v139
	v_pk_mul_f32 v[138:139], v[46:47], v[124:125]
	s_nop 0
	v_fma_f32 v138, v140, v137, v138
	v_pk_mul_f32 v[140:141], v[96:97], v[126:127]
	v_fmac_f32_e32 v139, v152, v138
	v_exp_f32_e32 v153, v140
	v_exp_f32_e32 v154, v141
	v_pk_mul_f32 v[140:141], v[48:49], v[126:127]
	s_nop 0
	v_fma_f32 v140, v153, v139, v140
	v_fmac_f32_e32 v141, v154, v140
	v_cmp_nlt_f32_e64 vcc, |v141|, s10
	s_cbranch_vccz .LBB3_5
	v_cmp_lt_f32_e32 vcc, s11, v18
	v_cvt_f32_f16_e32 v118, v151
	s_nop 0
	v_cndmask_b32_e32 v18, v112, v18, vcc
	v_cmp_lt_f32_e32 vcc, s11, v19
	s_nop 1
	v_cndmask_b32_e32 v19, v113, v19, vcc
	v_pk_mul_f32 v[112:113], v[96:97], v[18:19]
	v_cmp_lt_f32_e32 vcc, s11, v20
	v_exp_f32_e32 v112, v112
	v_exp_f32_e32 v113, v113
	v_cndmask_b32_e32 v20, v34, v20, vcc
	v_cmp_lt_f32_e32 vcc, s11, v21
	v_pk_mul_f32 v[18:19], v[78:79], v[18:19]
	s_nop 0
	v_cndmask_b32_e32 v21, v35, v21, vcc
	v_pk_mul_f32 v[34:35], v[96:97], v[20:21]
	v_fma_f32 v18, v112, v118, v18
	v_exp_f32_e32 v34, v34
	v_fmac_f32_e32 v19, v113, v18
	v_cmp_lt_f32_e32 vcc, s11, v22
	v_pk_mul_f32 v[78:79], v[2:3], v[18:19]
	v_pk_mul_f32 v[2:3], v[36:37], v[20:21]
	v_cndmask_b32_e32 v18, v80, v22, vcc
	v_cmp_lt_f32_e32 vcc, s11, v23
	v_exp_f32_e32 v35, v35
	v_fma_f32 v2, v34, v19, v2
	v_cndmask_b32_e32 v19, v81, v23, vcc
	v_pk_mul_f32 v[20:21], v[96:97], v[18:19]
	v_fmac_f32_e32 v3, v35, v2
	v_exp_f32_e32 v20, v20
	v_cmp_lt_f32_e32 vcc, s11, v24
	v_pk_mul_f32 v[80:81], v[4:5], v[2:3]
	v_pk_mul_f32 v[4:5], v[38:39], v[18:19]
	v_cndmask_b32_e32 v2, v114, v24, vcc
	v_cmp_lt_f32_e32 vcc, s11, v25
	v_exp_f32_e32 v21, v21
	v_fma_f32 v4, v20, v3, v4
	v_cndmask_b32_e32 v3, v115, v25, vcc
	v_pk_mul_f32 v[18:19], v[96:97], v[2:3]
	v_fmac_f32_e32 v5, v21, v4
	v_exp_f32_e32 v18, v18
	v_cmp_lt_f32_e32 vcc, s11, v26
	v_pk_mul_f32 v[112:113], v[6:7], v[4:5]
	v_pk_mul_f32 v[2:3], v[40:41], v[2:3]
	v_cndmask_b32_e32 v4, v116, v26, vcc
	v_cmp_lt_f32_e32 vcc, s11, v27
	v_exp_f32_e32 v19, v19
	v_fma_f32 v2, v18, v5, v2
	v_cndmask_b32_e32 v5, v117, v27, vcc
	v_pk_mul_f32 v[6:7], v[96:97], v[4:5]
	v_fmac_f32_e32 v3, v19, v2
	v_exp_f32_e32 v6, v6
	v_exp_f32_e32 v7, v7
	v_cmp_lt_f32_e32 vcc, s11, v28
	v_pk_mul_f32 v[114:115], v[8:9], v[2:3]
	v_pk_mul_f32 v[4:5], v[42:43], v[4:5]
	v_cndmask_b32_e32 v2, v120, v28, vcc
	v_cmp_lt_f32_e32 vcc, s11, v29
	v_fma_f32 v4, v6, v3, v4
	v_fmac_f32_e32 v5, v7, v4
	v_cndmask_b32_e32 v3, v121, v29, vcc
	v_pk_mul_f32 v[6:7], v[96:97], v[2:3]
	v_cmp_lt_f32_e32 vcc, s11, v30
	v_exp_f32_e32 v6, v6
	v_exp_f32_e32 v7, v7
	v_pk_mul_f32 v[116:117], v[10:11], v[4:5]
	v_pk_mul_f32 v[2:3], v[44:45], v[2:3]
	v_cndmask_b32_e32 v4, v124, v30, vcc
	v_cmp_lt_f32_e32 vcc, s11, v31
	v_fma_f32 v2, v6, v5, v2
	v_fmac_f32_e32 v3, v7, v2
	v_cndmask_b32_e32 v5, v125, v31, vcc
	v_pk_mul_f32 v[6:7], v[96:97], v[4:5]
	v_cmp_lt_f32_e32 vcc, s11, v32
	v_exp_f32_e32 v6, v6
	v_exp_f32_e32 v7, v7
	v_pk_mul_f32 v[118:119], v[12:13], v[2:3]
	v_pk_mul_f32 v[4:5], v[46:47], v[4:5]
	v_cndmask_b32_e32 v2, v126, v32, vcc
	v_cmp_lt_f32_e32 vcc, s11, v33
	v_fma_f32 v4, v6, v3, v4
	v_fmac_f32_e32 v5, v7, v4
	v_cndmask_b32_e32 v3, v127, v33, vcc
	v_pk_mul_f32 v[6:7], v[96:97], v[2:3]
	v_pk_mul_f32 v[2:3], v[48:49], v[2:3]
	v_exp_f32_e32 v6, v6
	v_exp_f32_e32 v7, v7
	v_pk_mul_f32 v[120:121], v[14:15], v[4:5]
	v_fma_f32 v2, v6, v5, v2
	v_fmac_f32_e32 v3, v7, v2
	v_pk_mul_f32 v[124:125], v[16:17], v[2:3]
	v_cvt_f32_f16_e32 v138, v150
	v_mfma_f32_32x32x16_f16 v[34:49], v[74:77], v[70:73], 0
	v_mfma_f32_32x32x16_f16 v[18:33], v[74:77], v[54:57], 0
	s_nop 10
	s_branch .Lp3_6b
.LBB3_5:
	v_mfma_f32_32x32x16_f16 v[34:49], v[74:77], v[70:73], 0
	v_mfma_f32_32x32x16_f16 v[18:33], v[74:77], v[54:57], 0
	v_pk_mul_f32 v[78:79], v[2:3], v[118:119]
	v_pk_mul_f32 v[80:81], v[4:5], v[128:129]
	v_pk_mul_f32 v[112:113], v[6:7], v[130:131]
	v_pk_mul_f32 v[114:115], v[8:9], v[132:133]
	v_pk_mul_f32 v[116:117], v[10:11], v[134:135]
	v_pk_mul_f32 v[118:119], v[12:13], v[136:137]
	v_pk_mul_f32 v[120:121], v[14:15], v[138:139]
	v_pk_mul_f32 v[124:125], v[16:17], v[140:141]
	v_cvt_f32_f16_e32 v138, v150
	s_nop 1
.LBB3_6:
.Lp3_6b:
	v_max_i32_e32 v4, v34, v35
	v_exp_f32_e32 v2, v48
	v_exp_f32_e32 v3, v49
	v_max3_i32 v4, v4, v36, v37
	v_max3_i32 v4, v4, v38, v39
	v_max3_i32 v4, v4, v40, v41
	v_max3_i32 v4, v4, v42, v43
	v_pk_add_f32 v[2:3], v[2:3], 1.0 op_sel_hi:[1,0]
	v_max3_i32 v4, v4, v44, v45
	v_log_f32_e32 v136, v2
	v_max3_i32 v2, v4, v46, v47
	v_max3_i32 v2, v2, v48, v49
	v_log_f32_e32 v137, v3
	v_cmp_lt_i32_e32 vcc, s11, v2
	v_mfma_f32_32x32x16_f16 v[2:17], v[74:77], v[50:53], 0
	v_exp_f32_e32 v134, v46
	v_exp_f32_e32 v135, v47
	v_exp_f32_e32 v132, v44
	v_exp_f32_e32 v133, v45
	v_exp_f32_e32 v130, v42
	v_exp_f32_e32 v131, v43
	v_exp_f32_e32 v128, v40
	v_exp_f32_e32 v129, v41
	v_exp_f32_e32 v126, v38
	v_exp_f32_e32 v127, v39
	v_exp_f32_e32 v76, v36
	v_exp_f32_e32 v77, v37
	v_exp_f32_e32 v74, v34
	v_exp_f32_e32 v75, v35
	v_pk_mul_f32 v[18:19], v[122:123], v[18:19]
	s_cbranch_vccz .LBB3_8
	v_cmp_lt_f32_e32 vcc, s11, v48
	v_pk_mul_f32 v[140:141], v[110:111], v[32:33]
	v_pk_mul_f32 v[150:151], v[108:109], v[30:31]
	v_cndmask_b32_e32 v122, v136, v48, vcc
	v_cmp_lt_f32_e32 vcc, s11, v49
	v_pk_mul_f32 v[152:153], v[106:107], v[28:29]
	v_pk_mul_f32 v[154:155], v[104:105], v[26:27]
	v_cndmask_b32_e32 v123, v137, v49, vcc
	v_pk_mul_f32 v[48:49], v[92:93], v[122:123]
	v_pk_mul_f32 v[122:123], v[140:141], v[122:123]
	v_exp_f32_e32 v160, v49
	v_exp_f32_e32 v139, v48
	v_pk_add_f32 v[140:141], v[134:135], 1.0 op_sel_hi:[1,0]
	v_cmp_lt_f32_e32 vcc, s11, v46
	v_fma_f32 v123, v160, v138, v123
	v_log_f32_e32 v140, v140
	v_fmac_f32_e32 v122, v139, v123
	v_log_f32_e32 v139, v141
	v_pk_mul_f32 v[156:157], v[102:103], v[24:25]
	v_cndmask_b32_e32 v140, v140, v46, vcc
	v_cmp_lt_f32_e32 vcc, s11, v47
	v_pk_mul_f32 v[158:159], v[100:101], v[22:23]
	v_pk_mul_f32 v[48:49], v[98:99], v[20:21]
	v_cndmask_b32_e32 v141, v139, v47, vcc
	v_pk_mul_f32 v[160:161], v[92:93], v[140:141]
	v_pk_mul_f32 v[140:141], v[150:151], v[140:141]
	v_exp_f32_e32 v139, v161
	v_pk_fma_f32 v[46:47], v[16:17], v[122:123], v[124:125]
	v_cmp_lt_f32_e32 vcc, s11, v44
	v_exp_f32_e32 v160, v160
	v_fma_f32 v141, v139, v122, v141
	v_pk_add_f32 v[122:123], v[132:133], 1.0 op_sel_hi:[1,0]
	s_nop 0
	v_log_f32_e32 v122, v122
	v_log_f32_e32 v123, v123
	v_fmac_f32_e32 v140, v160, v141
	v_cndmask_b32_e32 v122, v122, v44, vcc
	v_cmp_lt_f32_e32 vcc, s11, v45
	s_nop 1
	v_cndmask_b32_e32 v123, v123, v45, vcc
	v_pk_mul_f32 v[150:151], v[92:93], v[122:123]
	v_pk_mul_f32 v[122:123], v[152:153], v[122:123]
	v_exp_f32_e32 v139, v151
	v_pk_fma_f32 v[44:45], v[14:15], v[140:141], v[120:121]
	v_exp_f32_e32 v150, v150
	v_cmp_lt_f32_e32 vcc, s11, v42
	v_fma_f32 v123, v139, v140, v123
	v_pk_add_f32 v[140:141], v[130:131], 1.0 op_sel_hi:[1,0]
	v_fmac_f32_e32 v122, v150, v123
	v_log_f32_e32 v139, v140
	v_log_f32_e32 v141, v141
	v_cndmask_b32_e32 v140, v139, v42, vcc
	v_cmp_lt_f32_e32 vcc, s11, v43
	s_nop 1
	v_cndmask_b32_e32 v141, v141, v43, vcc
	v_pk_mul_f32 v[150:151], v[92:93], v[140:141]
	v_pk_mul_f32 v[140:141], v[154:155], v[140:141]
	v_exp_f32_e32 v139, v151
	v_pk_fma_f32 v[42:43], v[12:13], v[122:123], v[118:119]
	v_exp_f32_e32 v150, v150
	v_cmp_lt_f32_e32 vcc, s11, v40
	v_fma_f32 v141, v139, v122, v141
	v_pk_add_f32 v[122:123], v[128:129], 1.0 op_sel_hi:[1,0]
	v_fmac_f32_e32 v140, v150, v141
	v_log_f32_e32 v122, v122
	v_log_f32_e32 v123, v123
	v_cndmask_b32_e32 v122, v122, v40, vcc
	v_cmp_lt_f32_e32 vcc, s11, v41
	s_nop 1
	v_cndmask_b32_e32 v123, v123, v41, vcc
	v_pk_mul_f32 v[150:151], v[92:93], v[122:123]
	v_pk_mul_f32 v[122:123], v[156:157], v[122:123]
	v_exp_f32_e32 v139, v151
	v_pk_fma_f32 v[40:41], v[10:11], v[140:141], v[116:117]
	v_exp_f32_e32 v150, v150
	v_cmp_lt_f32_e32 vcc, s11, v38
	v_fma_f32 v123, v139, v140, v123
	v_pk_add_f32 v[140:141], v[126:127], 1.0 op_sel_hi:[1,0]
	v_fmac_f32_e32 v122, v150, v123
	v_log_f32_e32 v139, v140
	v_log_f32_e32 v141, v141
	v_cndmask_b32_e32 v140, v139, v38, vcc
	v_cmp_lt_f32_e32 vcc, s11, v39
	s_nop 1
	v_cndmask_b32_e32 v141, v141, v39, vcc
	v_pk_mul_f32 v[150:151], v[92:93], v[140:141]
	v_pk_mul_f32 v[140:141], v[158:159], v[140:141]
	v_exp_f32_e32 v139, v151
	v_pk_fma_f32 v[38:39], v[8:9], v[122:123], v[114:115]
	v_cmp_lt_f32_e32 vcc, s11, v36
	v_exp_f32_e32 v150, v150
	v_fma_f32 v141, v139, v122, v141
	v_pk_add_f32 v[122:123], v[76:77], 1.0 op_sel_hi:[1,0]
	v_fmac_f32_e32 v140, v150, v141
	v_log_f32_e32 v122, v122
	v_log_f32_e32 v123, v123
	v_cndmask_b32_e32 v122, v122, v36, vcc
	v_cmp_lt_f32_e32 vcc, s11, v37
	s_nop 1
	v_cndmask_b32_e32 v123, v123, v37, vcc
	v_pk_mul_f32 v[36:37], v[92:93], v[122:123]
	v_pk_mul_f32 v[48:49], v[48:49], v[122:123]
	v_exp_f32_e32 v139, v37
	v_exp_f32_e32 v150, v36
	v_pk_fma_f32 v[36:37], v[6:7], v[140:141], v[112:113]
	v_cmp_lt_f32_e32 vcc, s11, v34
	v_fma_f32 v49, v139, v140, v49
	v_pk_add_f32 v[140:141], v[74:75], 1.0 op_sel_hi:[1,0]
	v_fmac_f32_e32 v48, v150, v49
	v_log_f32_e32 v139, v140
	v_pk_fma_f32 v[122:123], v[4:5], v[48:49], v[80:81]
	v_log_f32_e32 v49, v141
	v_cndmask_b32_e32 v34, v139, v34, vcc
	v_cmp_lt_f32_e32 vcc, s11, v35
	s_nop 1
	v_cndmask_b32_e32 v35, v49, v35, vcc
	s_cbranch_execnz .LBB3_2
	s_branch .LBB3_9

.LBB3_12:
	s_nop 0
	v_mfma_f32_32x32x16_f16 v[2:17], v[18:21], v[66:69], 0
	v_add_u32_e32 v137, s6, v134
	v_lshl_add_u32 v136, v137, 2, v1
	ds_read_b128 v[86:89], v136
	ds_read_b128 v[82:85], v136 offset:16
	ds_read_b128 v[78:81], v136 offset:32
	ds_read_b128 v[74:77], v136 offset:48
	s_nop 5
	v_exp_f32_e32 v22, v2
	v_exp_f32_e32 v23, v3
	v_mfma_f32_32x32x16_f16 v[34:49], v[18:21], v[54:57], 0
	v_exp_f32_e32 v104, v4
	v_exp_f32_e32 v105, v5
	v_pk_add_f32 v[22:23], v[22:23], 1.0 op_sel_hi:[1,0]
	v_exp_f32_e32 v112, v10
	v_log_f32_e32 v100, v22
	v_log_f32_e32 v101, v23
	v_exp_f32_e32 v113, v11
	s_waitcnt lgkmcnt(3)
	s_nop 3
	v_pk_mul_f32 v[102:103], v[86:87], v[34:35]
	v_pk_add_f32 v[34:35], v[104:105], 1.0 op_sel_hi:[1,0]
	v_pk_mul_f32 v[22:23], v[96:97], v[100:101]
	v_log_f32_e32 v34, v34
	v_exp_f32_e32 v106, v22
	v_log_f32_e32 v35, v35
	v_exp_f32_e32 v107, v23
	v_pk_mul_f32 v[110:111], v[102:103], v[100:101]
	v_pk_mul_f32 v[36:37], v[88:89], v[36:37]
	v_fma_mix_f32 v110, v106, v139, v110 op_sel_hi:[0,1,0]
	v_pk_mul_f32 v[104:105], v[96:97], v[34:35]
	v_fmac_f32_e32 v111, v107, v110
	v_exp_f32_e32 v104, v104
	v_exp_f32_e32 v106, v6
	v_exp_f32_e32 v107, v7
	v_pk_mul_f32 v[118:119], v[36:37], v[34:35]
	v_exp_f32_e32 v108, v105
	v_fma_f32 v118, v104, v111, v118
	v_pk_add_f32 v[104:105], v[106:107], 1.0 op_sel_hi:[1,0]
	v_exp_f32_e32 v106, v8
	v_log_f32_e32 v104, v104
	v_log_f32_e32 v105, v105
	v_exp_f32_e32 v107, v9
	v_fmac_f32_e32 v119, v108, v118
	s_waitcnt lgkmcnt(2)
	v_pk_mul_f32 v[38:39], v[82:83], v[38:39]
	v_pk_mul_f32 v[108:109], v[96:97], v[104:105]
	v_pk_add_f32 v[106:107], v[106:107], 1.0 op_sel_hi:[1,0]
	v_exp_f32_e32 v108, v108
	v_exp_f32_e32 v109, v109
	v_log_f32_e32 v106, v106
	v_log_f32_e32 v107, v107
	v_pk_mul_f32 v[120:121], v[38:39], v[104:105]
	v_pk_mul_f32 v[40:41], v[84:85], v[40:41]
	v_fma_f32 v120, v108, v119, v120
	v_fmac_f32_e32 v121, v109, v120
	v_pk_mul_f32 v[108:109], v[96:97], v[106:107]
	v_pk_mul_f32 v[122:123], v[40:41], v[106:107]
	v_exp_f32_e32 v108, v108
	v_exp_f32_e32 v114, v109
	s_waitcnt lgkmcnt(1)
	v_pk_mul_f32 v[42:43], v[78:79], v[42:43]
	v_exp_f32_e32 v116, v14
	v_fma_f32 v122, v108, v121, v122
	v_pk_add_f32 v[108:109], v[112:113], 1.0 op_sel_hi:[1,0]
	v_exp_f32_e32 v112, v12
	v_log_f32_e32 v108, v108
	v_log_f32_e32 v109, v109
	v_exp_f32_e32 v113, v13
	v_fmac_f32_e32 v123, v114, v122
	v_exp_f32_e32 v117, v15
	v_pk_mul_f32 v[114:115], v[96:97], v[108:109]
	v_pk_add_f32 v[112:113], v[112:113], 1.0 op_sel_hi:[1,0]
	v_exp_f32_e32 v114, v114
	v_exp_f32_e32 v115, v115
	v_log_f32_e32 v112, v112
	v_log_f32_e32 v113, v113
	v_pk_mul_f32 v[124:125], v[42:43], v[108:109]
	v_pk_mul_f32 v[44:45], v[80:81], v[44:45]
	v_fma_f32 v124, v114, v123, v124
	v_fmac_f32_e32 v125, v115, v124
	v_pk_mul_f32 v[114:115], v[96:97], v[112:113]
	v_pk_mul_f32 v[126:127], v[44:45], v[112:113]
	v_exp_f32_e32 v114, v114
	v_exp_f32_e32 v128, v115
	s_waitcnt lgkmcnt(0)
	v_pk_mul_f32 v[46:47], v[74:75], v[46:47]
	v_mfma_f32_32x32x16_f16 v[18:33], v[18:21], v[50:53], 0
	v_fma_f32 v126, v114, v125, v126
	v_add_f32_e64 v114, v116, 1.0
	v_add_f32_e64 v115, v117, 1.0
	v_exp_f32_e32 v116, v16
	v_log_f32_e32 v114, v114
	v_log_f32_e32 v115, v115
	v_exp_f32_e32 v117, v17
	v_fmac_f32_e32 v127, v128, v126
	v_pk_mul_f32 v[48:49], v[76:77], v[48:49]
	v_pk_mul_f32 v[128:129], v[96:97], v[114:115]
	v_pk_add_f32 v[116:117], v[116:117], 1.0 op_sel_hi:[1,0]
	v_exp_f32_e32 v130, v128
	v_log_f32_e32 v116, v116
	v_log_f32_e32 v117, v117
	v_exp_f32_e32 v140, v129
	v_pk_mul_f32 v[128:129], v[46:47], v[114:115]
	s_nop 0
	v_fma_f32 v128, v130, v127, v128
	v_pk_mul_f32 v[130:131], v[96:97], v[116:117]
	v_fmac_f32_e32 v129, v140, v128
	v_exp_f32_e32 v141, v130
	v_exp_f32_e32 v142, v131
	v_pk_mul_f32 v[130:131], v[48:49], v[116:117]
	s_nop 0
	v_fma_f32 v130, v141, v129, v130
	v_fmac_f32_e32 v131, v142, v130
	v_cmp_nlt_f32_e64 vcc, |v131|, s4
	s_cbranch_vccz .LBB3_14
	v_cmp_lt_f32_e32 vcc, s5, v2
	v_cvt_f32_f16_e32 v110, v139
	s_nop 0
	v_cndmask_b32_e32 v2, v100, v2, vcc
	v_cmp_lt_f32_e32 vcc, s5, v3
	s_nop 1
	v_cndmask_b32_e32 v3, v101, v3, vcc
	v_pk_mul_f32 v[100:101], v[96:97], v[2:3]
	v_cmp_lt_f32_e32 vcc, s5, v4
	v_exp_f32_e32 v100, v100
	v_exp_f32_e32 v101, v101
	v_cndmask_b32_e32 v4, v34, v4, vcc
	v_cmp_lt_f32_e32 vcc, s5, v5
	v_pk_mul_f32 v[2:3], v[102:103], v[2:3]
	s_nop 0
	v_cndmask_b32_e32 v5, v35, v5, vcc
	v_pk_mul_f32 v[34:35], v[96:97], v[4:5]
	v_fma_f32 v2, v100, v110, v2
	v_exp_f32_e32 v34, v34
	v_fmac_f32_e32 v3, v101, v2
	v_cmp_lt_f32_e32 vcc, s5, v6
	v_pk_mul_f32 v[100:101], v[18:19], v[2:3]
	v_pk_mul_f32 v[4:5], v[36:37], v[4:5]
	v_cndmask_b32_e32 v2, v104, v6, vcc
	v_cmp_lt_f32_e32 vcc, s5, v7
	v_exp_f32_e32 v35, v35
	v_fma_f32 v4, v34, v3, v4
	v_cndmask_b32_e32 v3, v105, v7, vcc
	v_pk_mul_f32 v[6:7], v[96:97], v[2:3]
	v_fmac_f32_e32 v5, v35, v4
	v_exp_f32_e32 v6, v6
	v_exp_f32_e32 v7, v7
	v_cmp_lt_f32_e32 vcc, s5, v8
	v_pk_mul_f32 v[102:103], v[20:21], v[4:5]
	v_pk_mul_f32 v[2:3], v[38:39], v[2:3]
	v_cndmask_b32_e32 v4, v106, v8, vcc
	v_cmp_lt_f32_e32 vcc, s5, v9
	v_fma_f32 v2, v6, v5, v2
	v_fmac_f32_e32 v3, v7, v2
	v_cndmask_b32_e32 v5, v107, v9, vcc
	v_pk_mul_f32 v[6:7], v[96:97], v[4:5]
	v_cmp_lt_f32_e32 vcc, s5, v10
	v_exp_f32_e32 v6, v6
	v_exp_f32_e32 v7, v7
	v_pk_mul_f32 v[104:105], v[22:23], v[2:3]
	v_pk_mul_f32 v[4:5], v[40:41], v[4:5]
	v_cndmask_b32_e32 v2, v108, v10, vcc
	v_cmp_lt_f32_e32 vcc, s5, v11
	v_fma_f32 v4, v6, v3, v4
	v_fmac_f32_e32 v5, v7, v4
	v_cndmask_b32_e32 v3, v109, v11, vcc
	v_pk_mul_f32 v[6:7], v[96:97], v[2:3]
	v_cmp_lt_f32_e32 vcc, s5, v12
	v_exp_f32_e32 v6, v6
	v_exp_f32_e32 v7, v7
	v_pk_mul_f32 v[106:107], v[24:25], v[4:5]
	v_pk_mul_f32 v[2:3], v[42:43], v[2:3]
	v_cndmask_b32_e32 v4, v112, v12, vcc
	v_cmp_lt_f32_e32 vcc, s5, v13
	v_fma_f32 v2, v6, v5, v2
	v_fmac_f32_e32 v3, v7, v2
	v_cndmask_b32_e32 v5, v113, v13, vcc
	v_pk_mul_f32 v[6:7], v[96:97], v[4:5]
	v_cmp_lt_f32_e32 vcc, s5, v14
	v_exp_f32_e32 v6, v6
	v_exp_f32_e32 v7, v7
	v_pk_mul_f32 v[108:109], v[26:27], v[2:3]
	v_pk_mul_f32 v[4:5], v[44:45], v[4:5]
	v_cndmask_b32_e32 v2, v114, v14, vcc
	v_cmp_lt_f32_e32 vcc, s5, v15
	v_fma_f32 v4, v6, v3, v4
	v_fmac_f32_e32 v5, v7, v4
	v_cndmask_b32_e32 v3, v115, v15, vcc
	v_pk_mul_f32 v[6:7], v[96:97], v[2:3]
	v_cmp_lt_f32_e32 vcc, s5, v16
	v_exp_f32_e32 v6, v6
	v_exp_f32_e32 v7, v7
	v_pk_mul_f32 v[110:111], v[28:29], v[4:5]
	v_pk_mul_f32 v[2:3], v[46:47], v[2:3]
	v_cndmask_b32_e32 v4, v116, v16, vcc
	v_cmp_lt_f32_e32 vcc, s5, v17
	v_fma_f32 v2, v6, v5, v2
	v_fmac_f32_e32 v3, v7, v2
	v_cndmask_b32_e32 v5, v117, v17, vcc
	v_pk_mul_f32 v[6:7], v[96:97], v[4:5]
	v_pk_mul_f32 v[4:5], v[48:49], v[4:5]
	v_exp_f32_e32 v6, v6
	v_exp_f32_e32 v7, v7
	v_pk_mul_f32 v[112:113], v[30:31], v[2:3]
	v_fma_f32 v4, v6, v3, v4
	v_fmac_f32_e32 v5, v7, v4
	v_pk_mul_f32 v[114:115], v[32:33], v[4:5]
	v_cvt_f32_f16_e32 v130, v138
	v_mfma_f32_32x32x16_f16 v[34:49], v[90:93], v[70:73], 0
	v_mfma_f32_32x32x16_f16 v[18:33], v[90:93], v[54:57], 0
	s_nop 10
	s_branch .Lp3_15b
.LBB3_14:
	v_mfma_f32_32x32x16_f16 v[34:49], v[90:93], v[70:73], 0
	v_pk_mul_f32 v[100:101], v[18:19], v[110:111]
	v_pk_mul_f32 v[102:103], v[20:21], v[118:119]
	v_pk_mul_f32 v[104:105], v[22:23], v[120:121]
	v_pk_mul_f32 v[106:107], v[24:25], v[122:123]
	v_pk_mul_f32 v[108:109], v[26:27], v[124:125]
	v_pk_mul_f32 v[110:111], v[28:29], v[126:127]
	v_pk_mul_f32 v[112:113], v[30:31], v[128:129]
	v_pk_mul_f32 v[114:115], v[32:33], v[130:131]
	v_cvt_f32_f16_e32 v130, v138
	v_mfma_f32_32x32x16_f16 v[18:33], v[90:93], v[54:57], 0
	s_nop 1
.LBB3_15:
.Lp3_15b:
	v_max_i32_e32 v4, v34, v35
	v_exp_f32_e32 v2, v48
	v_exp_f32_e32 v3, v49
	v_max3_i32 v4, v4, v36, v37
	v_max3_i32 v4, v4, v38, v39
	v_max3_i32 v4, v4, v40, v41
	v_max3_i32 v4, v4, v42, v43
	v_pk_add_f32 v[2:3], v[2:3], 1.0 op_sel_hi:[1,0]
	v_max3_i32 v4, v4, v44, v45
	v_log_f32_e32 v126, v2
	v_max3_i32 v2, v4, v46, v47
	v_max3_i32 v2, v2, v48, v49
	v_log_f32_e32 v127, v3
	v_cmp_lt_i32_e32 vcc, s5, v2
	v_mfma_f32_32x32x16_f16 v[2:17], v[90:93], v[50:53], 0
	v_exp_f32_e32 v124, v46
	v_exp_f32_e32 v125, v47
	v_exp_f32_e32 v122, v44
	v_exp_f32_e32 v123, v45
	v_exp_f32_e32 v120, v42
	v_exp_f32_e32 v121, v43
	v_exp_f32_e32 v118, v40
	v_exp_f32_e32 v119, v41
	v_exp_f32_e32 v116, v38
	v_exp_f32_e32 v117, v39
	v_exp_f32_e32 v92, v36
	v_exp_f32_e32 v93, v37
	v_exp_f32_e32 v90, v34
	v_exp_f32_e32 v91, v35
	v_pk_mul_f32 v[18:19], v[86:87], v[18:19]
	s_cbranch_vccz .LBB3_17
	v_cmp_lt_f32_e32 vcc, s5, v48
	v_pk_mul_f32 v[138:139], v[76:77], v[32:33]
	v_pk_mul_f32 v[140:141], v[74:75], v[30:31]
	v_cndmask_b32_e32 v128, v126, v48, vcc
	v_cmp_lt_f32_e32 vcc, s5, v49
	v_pk_mul_f32 v[142:143], v[80:81], v[28:29]
	v_pk_mul_f32 v[144:145], v[78:79], v[26:27]
	v_cndmask_b32_e32 v129, v127, v49, vcc
	v_pk_mul_f32 v[48:49], v[98:99], v[128:129]
	v_pk_mul_f32 v[128:129], v[138:139], v[128:129]
	v_exp_f32_e32 v150, v49
	v_exp_f32_e32 v131, v48
	v_pk_add_f32 v[138:139], v[124:125], 1.0 op_sel_hi:[1,0]
	v_cmp_lt_f32_e32 vcc, s5, v46
	v_fma_f32 v129, v150, v130, v129
	v_log_f32_e32 v138, v138
	v_fmac_f32_e32 v128, v131, v129
	v_log_f32_e32 v131, v139
	v_pk_mul_f32 v[146:147], v[84:85], v[24:25]
	v_cndmask_b32_e32 v138, v138, v46, vcc
	v_cmp_lt_f32_e32 vcc, s5, v47
	v_pk_mul_f32 v[148:149], v[82:83], v[22:23]
	v_pk_mul_f32 v[48:49], v[88:89], v[20:21]
	v_cndmask_b32_e32 v139, v131, v47, vcc
	v_pk_mul_f32 v[150:151], v[98:99], v[138:139]
	v_pk_mul_f32 v[138:139], v[140:141], v[138:139]
	v_exp_f32_e32 v131, v151
	v_pk_fma_f32 v[46:47], v[16:17], v[128:129], v[114:115]
	v_cmp_lt_f32_e32 vcc, s5, v44
	v_exp_f32_e32 v150, v150
	v_fma_f32 v139, v131, v128, v139
	v_pk_add_f32 v[128:129], v[122:123], 1.0 op_sel_hi:[1,0]
	s_nop 0
	v_log_f32_e32 v128, v128
	v_log_f32_e32 v129, v129
	v_fmac_f32_e32 v138, v150, v139
	v_cndmask_b32_e32 v128, v128, v44, vcc
	v_cmp_lt_f32_e32 vcc, s5, v45
	s_nop 1
	v_cndmask_b32_e32 v129, v129, v45, vcc
	v_pk_mul_f32 v[140:141], v[98:99], v[128:129]
	v_pk_mul_f32 v[128:129], v[142:143], v[128:129]
	v_exp_f32_e32 v131, v141
	v_pk_fma_f32 v[44:45], v[14:15], v[138:139], v[112:113]
	v_exp_f32_e32 v140, v140
	v_cmp_lt_f32_e32 vcc, s5, v42
	v_fma_f32 v129, v131, v138, v129
	v_pk_add_f32 v[138:139], v[120:121], 1.0 op_sel_hi:[1,0]
	v_fmac_f32_e32 v128, v140, v129
	v_log_f32_e32 v131, v138
	v_log_f32_e32 v139, v139
	v_cndmask_b32_e32 v138, v131, v42, vcc
	v_cmp_lt_f32_e32 vcc, s5, v43
	s_nop 1
	v_cndmask_b32_e32 v139, v139, v43, vcc
	v_pk_mul_f32 v[140:141], v[98:99], v[138:139]
	v_pk_mul_f32 v[138:139], v[144:145], v[138:139]
	v_exp_f32_e32 v131, v141
	v_pk_fma_f32 v[42:43], v[12:13], v[128:129], v[110:111]
	v_exp_f32_e32 v140, v140
	v_cmp_lt_f32_e32 vcc, s5, v40
	v_fma_f32 v139, v131, v128, v139
	v_pk_add_f32 v[128:129], v[118:119], 1.0 op_sel_hi:[1,0]
	v_fmac_f32_e32 v138, v140, v139
	v_log_f32_e32 v128, v128
	v_log_f32_e32 v129, v129
	v_cndmask_b32_e32 v128, v128, v40, vcc
	v_cmp_lt_f32_e32 vcc, s5, v41
	s_nop 1
	v_cndmask_b32_e32 v129, v129, v41, vcc
	v_pk_mul_f32 v[140:141], v[98:99], v[128:129]
	v_pk_mul_f32 v[128:129], v[146:147], v[128:129]
	v_exp_f32_e32 v131, v141
	v_pk_fma_f32 v[40:41], v[10:11], v[138:139], v[108:109]
	v_exp_f32_e32 v140, v140
	v_cmp_lt_f32_e32 vcc, s5, v38
	v_fma_f32 v129, v131, v138, v129
	v_pk_add_f32 v[138:139], v[116:117], 1.0 op_sel_hi:[1,0]
	v_fmac_f32_e32 v128, v140, v129
	v_log_f32_e32 v131, v138
	v_log_f32_e32 v139, v139
	v_cndmask_b32_e32 v138, v131, v38, vcc
	v_cmp_lt_f32_e32 vcc, s5, v39
	s_nop 1
	v_cndmask_b32_e32 v139, v139, v39, vcc
	v_pk_mul_f32 v[140:141], v[98:99], v[138:139]
	v_pk_mul_f32 v[138:139], v[148:149], v[138:139]
	v_exp_f32_e32 v131, v141
	v_pk_fma_f32 v[38:39], v[8:9], v[128:129], v[106:107]
	v_cmp_lt_f32_e32 vcc, s5, v36
	v_exp_f32_e32 v140, v140
	v_fma_f32 v139, v131, v128, v139
	v_pk_add_f32 v[128:129], v[92:93], 1.0 op_sel_hi:[1,0]
	v_fmac_f32_e32 v138, v140, v139
	v_log_f32_e32 v128, v128
	v_log_f32_e32 v129, v129
	v_cndmask_b32_e32 v128, v128, v36, vcc
	v_cmp_lt_f32_e32 vcc, s5, v37
	s_nop 1
	v_cndmask_b32_e32 v129, v129, v37, vcc
	v_pk_mul_f32 v[36:37], v[98:99], v[128:129]
	v_pk_mul_f32 v[48:49], v[48:49], v[128:129]
	v_exp_f32_e32 v131, v37
	v_exp_f32_e32 v140, v36
	v_pk_fma_f32 v[36:37], v[6:7], v[138:139], v[104:105]
	v_cmp_lt_f32_e32 vcc, s5, v34
	v_fma_f32 v49, v131, v138, v49
	v_pk_add_f32 v[138:139], v[90:91], 1.0 op_sel_hi:[1,0]
	v_fmac_f32_e32 v48, v140, v49
	v_log_f32_e32 v131, v138
	v_pk_fma_f32 v[128:129], v[4:5], v[48:49], v[102:103]
	v_log_f32_e32 v49, v139
	v_cndmask_b32_e32 v34, v131, v34, vcc
	v_cmp_lt_f32_e32 vcc, s5, v35
	s_nop 1
	v_cndmask_b32_e32 v35, v49, v35, vcc
	s_cbranch_execnz .LBB3_11
	s_branch .LBB3_18
